# SGU step 2: all LayerNorm gains and biases fetched with 16 wide loads up front instead of 32 serialized dword pairs; DATT full-tile block trimmed
# speedup vs baseline: 1.0058x; 1.0058x over previous
; #define LAS __attribute__((address_space(3)))
; __device__ __forceinline__ void datt_stream(LAS unsigned char* lds, const DattRun& c, const float C, const int wv) {
;     ...
;         if (do0) {
; #pragma unroll
;             for (int d0 = 0; d0 < 8; ++d0) { const bf16x8 b0 = *(const LAS bf16x8*)(Ks + ATT_KSWZ(r32, (d0 * 16 + hi * 8) * 2)); p0 = __builtin_amdgcn_mfma_f32_32x32x16_bf16(b0, qr[d0], p0, 0, 0, 0); } }
;         if (do1) {
; #pragma unroll
;             for (int d0 = 0; d0 < 8; ++d0) { const bf16x8 b1 = *(const LAS bf16x8*)(Ks + ATT_KSWZ(32 + r32, (d0 * 16 + hi * 8) * 2)); p1 = __builtin_amdgcn_mfma_f32_32x32x16_bf16(b1, qr[d0], p1, 0, 0, 0); } }
;         const int db = 64 * (rel - 1) - 32 * par - r32 + 4 * hi, qi = 64 * (c.a0 + pa) + 32 * par + r32; const unsigned L = (unsigned)c.L;
;         const LAS float* tb = c.tb + (db + 2 * HALFWIN);
;     ...
;         if (do0) DS_XFORM(p0, 0);
;         if (do1) DS_XFORM(p1, 32);
;     ...
;         float pmax = -__builtin_inff();
;         if (do0) {
; #pragma unroll
;             for (int r = 0; r < 16; ++r) pmax = fmaxf(pmax, p0[r]); }
;         if (do1) {
; #pragma unroll
;             for (int r = 0; r < 16; ++r) pmax = fmaxf(pmax, p1[r]); }
;         { auto rr = __builtin_amdgcn_permlane32_swap(__float_as_uint(pmax), __float_as_uint(pmax), false, false);
;           pmax = fmaxf(__uint_as_float(rr[0]), __uint_as_float(rr[1])); }
;         const float mn = fmaxf(m_reg, pmax), alpha = __builtin_amdgcn_exp2f(m_reg - mn); m_reg = mn;
.LBB0_430:
	s_cmp_eq_u32 s6, 3
	s_cbranch_scc1 .Lft0_old
	s_cmp_lg_u64 s[10:11], 0
	s_cbranch_scc1 .Lft0_old
	s_mov_b32 s12, 0x21500
	v_lshl_add_u32 v130, s62, 6, v239
	v_lshl_add_u32 v131, v130, 2, s12
	v_add_u32_e32 v64, v241, v219
	ds_read_b128 v[98:101], v64 offset:32768
	v_add_u32_e32 v135, v241, v215
	ds_read_b128 v[102:105], v135 offset:32768
	v_add_u32_e32 v138, v241, v186
	ds_read_b128 v[106:109], v138 offset:32768
	v_add_u32_e32 v139, v241, v233
	ds_read_b128 v[110:113], v139 offset:32768
	s_waitcnt lgkmcnt(3)
	v_mfma_f32_32x32x16_bf16 v[82:97], v[98:101], v[144:147], 0
	v_add_u32_e32 v140, v241, v234
	ds_read_b128 v[98:101], v140 offset:32768
	s_waitcnt lgkmcnt(3)
	v_mfma_f32_32x32x16_bf16 v[82:97], v[102:105], v[148:151], v[82:97]
	v_add_u32_e32 v141, v241, v235
	ds_read_b128 v[102:105], v141 offset:32768
	s_waitcnt lgkmcnt(3)
	v_mfma_f32_32x32x16_bf16 v[82:97], v[106:109], v[152:155], v[82:97]
	v_add_u32_e32 v142, v241, v236
	ds_read_b128 v[106:109], v142 offset:32768
	s_waitcnt lgkmcnt(3)
	v_mfma_f32_32x32x16_bf16 v[82:97], v[110:113], v[156:159], v[82:97]
	v_add_u32_e32 v143, v241, v237
	ds_read_b128 v[110:113], v143 offset:32768
	s_waitcnt lgkmcnt(3)
	v_mfma_f32_32x32x16_bf16 v[82:97], v[98:101], v[160:163], v[82:97]
	ds_read_b128 v[98:101], v64 offset:40960
	s_waitcnt lgkmcnt(3)
	v_mfma_f32_32x32x16_bf16 v[82:97], v[102:105], v[164:167], v[82:97]
	ds_read_b128 v[102:105], v135 offset:40960
	s_waitcnt lgkmcnt(3)
	v_mfma_f32_32x32x16_bf16 v[82:97], v[106:109], v[168:171], v[82:97]
	ds_read_b128 v[106:109], v138 offset:40960
	s_waitcnt lgkmcnt(3)
	v_mfma_f32_32x32x16_bf16 v[82:97], v[110:113], v[172:175], v[82:97]
	ds_read_b128 v[110:113], v139 offset:40960
	ds_read2_b32 v[114:115], v131 offset0:128 offset1:129
	ds_read2_b32 v[116:117], v131 offset0:130 offset1:131
	ds_read2_b32 v[118:119], v131 offset0:136 offset1:137
	ds_read2_b32 v[120:121], v131 offset0:138 offset1:139
	ds_read2_b32 v[122:123], v131 offset0:144 offset1:145
	ds_read2_b32 v[124:125], v131 offset0:146 offset1:147
	ds_read2_b32 v[126:127], v131 offset0:152 offset1:153
	ds_read2_b32 v[128:129], v131 offset0:154 offset1:155
	s_waitcnt lgkmcnt(11)
	v_mfma_f32_32x32x16_bf16 v[66:81], v[98:101], v[144:147], 0
	ds_read_b128 v[98:101], v140 offset:40960
	s_waitcnt lgkmcnt(11)
	v_mfma_f32_32x32x16_bf16 v[66:81], v[102:105], v[148:151], v[66:81]
	ds_read_b128 v[102:105], v141 offset:40960
	s_waitcnt lgkmcnt(11)
	v_mfma_f32_32x32x16_bf16 v[66:81], v[106:109], v[152:155], v[66:81]
	ds_read_b128 v[106:109], v142 offset:40960
	s_waitcnt lgkmcnt(11)
	v_mfma_f32_32x32x16_bf16 v[66:81], v[110:113], v[156:159], v[66:81]
	ds_read_b128 v[110:113], v143 offset:40960
	s_waitcnt lgkmcnt(3)
	v_mfma_f32_32x32x16_bf16 v[66:81], v[98:101], v[160:163], v[66:81]
	s_waitcnt lgkmcnt(2)
	v_mfma_f32_32x32x16_bf16 v[66:81], v[102:105], v[164:167], v[66:81]
	s_waitcnt lgkmcnt(1)
	v_mfma_f32_32x32x16_bf16 v[66:81], v[106:109], v[168:171], v[66:81]
	s_waitcnt lgkmcnt(0)
	v_mfma_f32_32x32x16_bf16 v[66:81], v[110:113], v[172:175], v[66:81]
	v_pk_fma_f32 v[82:83], v[82:83], s[94:95], v[114:115] op_sel_hi:[1,0,1]
	v_pk_fma_f32 v[84:85], v[84:85], s[94:95], v[116:117] op_sel_hi:[1,0,1]
	v_pk_fma_f32 v[86:87], v[86:87], s[94:95], v[118:119] op_sel_hi:[1,0,1]
	v_pk_fma_f32 v[88:89], v[88:89], s[94:95], v[120:121] op_sel_hi:[1,0,1]
	v_pk_fma_f32 v[90:91], v[90:91], s[94:95], v[122:123] op_sel_hi:[1,0,1]
	v_pk_fma_f32 v[92:93], v[92:93], s[94:95], v[124:125] op_sel_hi:[1,0,1]
	v_pk_fma_f32 v[94:95], v[94:95], s[94:95], v[126:127] op_sel_hi:[1,0,1]
	v_pk_fma_f32 v[96:97], v[96:97], s[94:95], v[128:129] op_sel_hi:[1,0,1]
	v_max_f32_e32 v132, v82, v83
	v_max3_f32 v132, v132, v84, v85
	v_max3_f32 v132, v132, v86, v87
	v_max3_f32 v132, v132, v88, v89
	v_max3_f32 v132, v132, v90, v91
	v_max3_f32 v132, v132, v92, v93
	v_max3_f32 v132, v132, v94, v95
	v_max3_f32 v132, v132, v96, v97
	ds_read2_b32 v[114:115], v131 offset0:160 offset1:161
	ds_read2_b32 v[116:117], v131 offset0:162 offset1:163
	ds_read2_b32 v[118:119], v131 offset0:168 offset1:169
	ds_read2_b32 v[120:121], v131 offset0:170 offset1:171
	ds_read2_b32 v[122:123], v131 offset0:176 offset1:177
	ds_read2_b32 v[124:125], v131 offset0:178 offset1:179
	ds_read2_b32 v[126:127], v131 offset0:184 offset1:185
	ds_read2_b32 v[128:129], v131 offset0:186 offset1:187
	ds_read_b64_tr_b16 v[98:99], v240 offset:0
	ds_read_b64_tr_b16 v[100:101], v240 offset:2048
	ds_read_b64_tr_b16 v[102:103], v240 offset:512
	ds_read_b64_tr_b16 v[104:105], v240 offset:2560
	ds_read_b64_tr_b16 v[106:107], v240 offset:4096
	ds_read_b64_tr_b16 v[108:109], v240 offset:6144
	s_waitcnt lgkmcnt(6)
	v_pk_fma_f32 v[66:67], v[66:67], s[94:95], v[114:115] op_sel_hi:[1,0,1]
	v_pk_fma_f32 v[68:69], v[68:69], s[94:95], v[116:117] op_sel_hi:[1,0,1]
	v_pk_fma_f32 v[70:71], v[70:71], s[94:95], v[118:119] op_sel_hi:[1,0,1]
	v_pk_fma_f32 v[72:73], v[72:73], s[94:95], v[120:121] op_sel_hi:[1,0,1]
	v_pk_fma_f32 v[74:75], v[74:75], s[94:95], v[122:123] op_sel_hi:[1,0,1]
	v_pk_fma_f32 v[76:77], v[76:77], s[94:95], v[124:125] op_sel_hi:[1,0,1]
	v_pk_fma_f32 v[78:79], v[78:79], s[94:95], v[126:127] op_sel_hi:[1,0,1]
	v_pk_fma_f32 v[80:81], v[80:81], s[94:95], v[128:129] op_sel_hi:[1,0,1]
	ds_read_b64_tr_b16 v[110:111], v240 offset:4608
	ds_read_b64_tr_b16 v[112:113], v240 offset:6656
	v_max3_f32 v132, v132, v66, v67
	v_max3_f32 v132, v132, v68, v69
	v_max3_f32 v132, v132, v70, v71
	v_max3_f32 v132, v132, v72, v73
	v_max3_f32 v132, v132, v74, v75
	v_max3_f32 v132, v132, v76, v77
	v_max3_f32 v132, v132, v78, v79
	v_max3_f32 v132, v132, v80, v81
	v_mov_b32_e32 v133, v132
	s_nop 1
	v_permlane32_swap_b32_e32 v132, v133
	v_max3_f32 v243, v245, v132, v133
	v_sub_f32_e32 v134, v243, v245
	v_cmp_lt_f32_e32 vcc, 0x41000000, v134
	s_cbranch_vccnz .Lft0_newmax
	v_mov_b32_e32 v243, v245

; __device__ __forceinline__ int crow(int r, int hi) { return (r & 3) + 8 * (r >> 2) + 4 * hi; }
; __device__ __forceinline__ void datt_stream(LAS unsigned char* lds, const DattRun& c, const float C, const int wv) {
;     ...
;             for (int r = 0; r < 16; ++r) { p0[r] = __builtin_amdgcn_exp2f(p0[r] - mn); ps += p0[r]; } }
;         if (do1) {
; #pragma unroll
;             for (int r = 0; r < 16; ++r) { p1[r] = __builtin_amdgcn_exp2f(p1[r] - mn); ps += p1[r]; } }
;         { auto rr = __builtin_amdgcn_permlane32_swap(__float_as_uint(ps), __float_as_uint(ps), false, false);
;           ps = __uint_as_float(rr[0]) + __uint_as_float(rr[1]); }
;         l_reg = l_reg * alpha + ps;
;         if (__any(alpha < 1.f)) { if (hi == 0) al_l[r32] = alpha; asm volatile("s_waitcnt lgkmcnt(0)" ::: "memory");
; #pragma unroll
;             for (int r = 0; r < 16; ++r) { const float a = al_l[crow(r, hi)];
; #pragma unroll
;                 for (int d = 0; d < 4; ++d) o[d][r] *= a; } }
;         const int vb = vb0 + b * SHM_T;
;     ...
;         if (do0) { bf16x8 pa0_, pa1_; DS_PK4(p0, 0, pa0_); DS_PK4(p0, 8, pa1_);
;             pv_half2<0, 1, 0>(o[0], o[1], vb, pa0_, pa1_); pv_half2<2, 3, 0>(o[2], o[3], vb, pa0_, pa1_); }
;         if (do1) { bf16x8 pa2_, pa3_; DS_PK4(p1, 0, pa2_); DS_PK4(p1, 8, pa3_);
;             pv_half2<0, 1, 1>(o[0], o[1], vb, pa2_, pa3_); pv_half2<2, 3, 1>(o[2], o[3], vb, pa2_, pa3_); }
.Lft0_noresc:
	v_permlane32_swap_b32_e32 v82, v84
	v_permlane32_swap_b32_e32 v83, v85
	v_permlane32_swap_b32_e32 v86, v88
	v_permlane32_swap_b32_e32 v87, v89
	v_pk_add_f32 v[66:67], v[66:67], v[132:133] neg_lo:[0,1] neg_hi:[0,1]
	v_pk_add_f32 v[68:69], v[68:69], v[132:133] neg_lo:[0,1] neg_hi:[0,1]
	v_pk_add_f32 v[70:71], v[70:71], v[132:133] neg_lo:[0,1] neg_hi:[0,1]
	v_pk_add_f32 v[72:73], v[72:73], v[132:133] neg_lo:[0,1] neg_hi:[0,1]
	v_pk_add_f32 v[74:75], v[74:75], v[132:133] neg_lo:[0,1] neg_hi:[0,1]
	v_pk_add_f32 v[76:77], v[76:77], v[132:133] neg_lo:[0,1] neg_hi:[0,1]
	v_pk_add_f32 v[78:79], v[78:79], v[132:133] neg_lo:[0,1] neg_hi:[0,1]
	v_pk_add_f32 v[80:81], v[80:81], v[132:133] neg_lo:[0,1] neg_hi:[0,1]
	v_exp_f32_e32 v66, v66
	v_exp_f32_e32 v67, v67
	v_exp_f32_e32 v68, v68
	v_exp_f32_e32 v69, v69
	v_exp_f32_e32 v70, v70
	v_exp_f32_e32 v71, v71
	v_exp_f32_e32 v72, v72
	v_exp_f32_e32 v73, v73
	v_exp_f32_e32 v74, v74
	v_exp_f32_e32 v75, v75
	v_exp_f32_e32 v76, v76
	v_exp_f32_e32 v77, v77
	v_exp_f32_e32 v78, v78
	v_exp_f32_e32 v79, v79
	v_exp_f32_e32 v80, v80
	v_exp_f32_e32 v81, v81
	v_pk_add_f32 v[136:137], v[136:137], v[66:67]
	v_pk_add_f32 v[136:137], v[136:137], v[68:69]
	v_pk_add_f32 v[136:137], v[136:137], v[70:71]
	v_pk_add_f32 v[136:137], v[136:137], v[72:73]
	v_pk_add_f32 v[136:137], v[136:137], v[74:75]
	v_pk_add_f32 v[136:137], v[136:137], v[76:77]
	v_pk_add_f32 v[136:137], v[136:137], v[78:79]
	v_pk_add_f32 v[136:137], v[136:137], v[80:81]
	v_add_f32_e32 v64, v136, v137
	s_waitcnt lgkmcnt(0)
	v_mfma_f32_32x32x16_bf16 v[0:15], v[82:85], v[98:101], v[0:15]
	ds_read_b64_tr_b16 v[98:99], v240 offset:8192
	ds_read_b64_tr_b16 v[100:101], v240 offset:10240
	v_mfma_f32_32x32x16_bf16 v[16:31], v[82:85], v[102:105], v[16:31]
	ds_read_b64_tr_b16 v[102:103], v240 offset:8704
	ds_read_b64_tr_b16 v[104:105], v240 offset:10752
	v_mfma_f32_32x32x16_bf16 v[0:15], v[86:89], v[106:109], v[0:15]
	ds_read_b64_tr_b16 v[106:107], v240 offset:12288
	ds_read_b64_tr_b16 v[108:109], v240 offset:14336
	v_mfma_f32_32x32x16_bf16 v[16:31], v[86:89], v[110:113], v[16:31]
	ds_read_b64_tr_b16 v[110:111], v240 offset:12800
	ds_read_b64_tr_b16 v[112:113], v240 offset:14848
	v_mfma_f32_32x32x16_bf16 v[32:47], v[82:85], v[114:117], v[32:47]
	ds_read_b64_tr_b16 v[114:115], v240 offset:9216
	ds_read_b64_tr_b16 v[116:117], v240 offset:11264
	v_mfma_f32_32x32x16_bf16 v[48:63], v[82:85], v[118:121], v[48:63]
	ds_read_b64_tr_b16 v[118:119], v240 offset:9728
	ds_read_b64_tr_b16 v[120:121], v240 offset:11776
	v_mfma_f32_32x32x16_bf16 v[32:47], v[86:89], v[122:125], v[32:47]
	ds_read_b64_tr_b16 v[122:123], v240 offset:13312
	ds_read_b64_tr_b16 v[124:125], v240 offset:15360
	v_mfma_f32_32x32x16_bf16 v[48:63], v[86:89], v[126:129], v[48:63]
	ds_read_b64_tr_b16 v[126:127], v240 offset:13824
	s_waitcnt lgkmcnt(14)
	ds_read_b64_tr_b16 v[128:129], v240 offset:15872
	v_cvt_pk_bf16_f32 v66, v66, v67
	v_cvt_pk_bf16_f32 v67, v68, v69
	v_cvt_pk_bf16_f32 v68, v70, v71
	v_cvt_pk_bf16_f32 v69, v72, v73
	v_cvt_pk_bf16_f32 v70, v74, v75
	v_cvt_pk_bf16_f32 v71, v76, v77
	v_cvt_pk_bf16_f32 v72, v78, v79
	v_cvt_pk_bf16_f32 v73, v80, v81
	v_mov_b32_e32 v244, v64
	v_permlane32_swap_b32_e32 v66, v68
	v_permlane32_swap_b32_e32 v67, v69
	v_permlane32_swap_b32_e32 v70, v72
	v_permlane32_swap_b32_e32 v71, v73
	v_permlane32_swap_b32_e32 v64, v244
	s_waitcnt lgkmcnt(14)
	v_mfma_f32_32x32x16_bf16 v[0:15], v[66:69], v[98:101], v[0:15]
	s_waitcnt lgkmcnt(12)
	v_mfma_f32_32x32x16_bf16 v[16:31], v[66:69], v[102:105], v[16:31]
	s_waitcnt lgkmcnt(10)
	v_mfma_f32_32x32x16_bf16 v[0:15], v[70:73], v[106:109], v[0:15]
	s_waitcnt lgkmcnt(8)
	v_mfma_f32_32x32x16_bf16 v[16:31], v[70:73], v[110:113], v[16:31]
	s_waitcnt lgkmcnt(6)
	v_mfma_f32_32x32x16_bf16 v[32:47], v[66:69], v[114:117], v[32:47]
	s_waitcnt lgkmcnt(4)
	v_mfma_f32_32x32x16_bf16 v[48:63], v[66:69], v[118:121], v[48:63]
	s_waitcnt lgkmcnt(2)
	v_mfma_f32_32x32x16_bf16 v[32:47], v[70:73], v[122:125], v[32:47]
	s_waitcnt lgkmcnt(0)
	v_mfma_f32_32x32x16_bf16 v[48:63], v[70:73], v[126:129], v[48:63]
	s_nop 1
	s_branch .LBB0_463

; #define LAS __attribute__((address_space(3)))
; __device__ __forceinline__ void datt_stream(LAS unsigned char* lds, const DattRun& c, const float C, const int wv) {
;     ...
;         const LAS unsigned char* Ks = K_lds + b * SHM_T;
;         if (do0) {
; #pragma unroll
;             for (int d0 = 0; d0 < 8; ++d0) { const bf16x8 b0 = *(const LAS bf16x8*)(Ks + ATT_KSWZ(r32, (d0 * 16 + hi * 8) * 2)); p0 = __builtin_amdgcn_mfma_f32_32x32x16_bf16(b0, qr[d0], p0, 0, 0, 0); } }
;         if (do1) {
; #pragma unroll
;             for (int d0 = 0; d0 < 8; ++d0) { const bf16x8 b1 = *(const LAS bf16x8*)(Ks + ATT_KSWZ(32 + r32, (d0 * 16 + hi * 8) * 2)); p1 = __builtin_amdgcn_mfma_f32_32x32x16_bf16(b1, qr[d0], p1, 0, 0, 0); } }
;         const int db = 64 * (rel - 1) - 32 * par - r32 + 4 * hi, qi = 64 * (c.a0 + pa) + 32 * par + r32; const unsigned L = (unsigned)c.L;
;         const LAS float* tb = c.tb + (db + 2 * HALFWIN);
;     ...
;         if (do0) DS_XFORM(p0, 0);
;         if (do1) DS_XFORM(p1, 32);
;     ...
;         float pmax = -__builtin_inff();
;         if (do0) {
; #pragma unroll
;             for (int r = 0; r < 16; ++r) pmax = fmaxf(pmax, p0[r]); }
;         if (do1) {
; #pragma unroll
;             for (int r = 0; r < 16; ++r) pmax = fmaxf(pmax, p1[r]); }
;         { auto rr = __builtin_amdgcn_permlane32_swap(__float_as_uint(pmax), __float_as_uint(pmax), false, false);
;           pmax = fmaxf(__uint_as_float(rr[0]), __uint_as_float(rr[1])); }
;         const float mn = fmaxf(m_reg, pmax), alpha = __builtin_amdgcn_exp2f(m_reg - mn); m_reg = mn;
.LBB0_485:
	s_cmp_lg_u32 s12, 2
	s_cselect_b64 s[8:9], -1, 0
	s_cmp_eq_u32 s12, 2
	v_add_u32_e32 v0, v241, v219
	v_add_u32_e32 v38, v241, v215
	v_add_u32_e32 v37, v241, v186
	v_add_u32_e32 v36, v241, v233
	v_add_u32_e32 v35, v241, v234
	v_add_u32_e32 v34, v241, v235
	v_add_u32_e32 v33, v241, v236
	v_add_u32_e32 v32, v241, v237
	s_cbranch_scc1 .LBB0_489
	s_cmp_eq_u32 s12, 3
	s_cbranch_scc1 .Lft1_old
	s_cmp_lg_u64 s[10:11], 0
	s_cbranch_scc1 .Lft1_old
	s_mov_b32 s12, 0x21500
	v_lshl_add_u32 v69, s63, 6, v239
	v_lshl_add_u32 v68, v69, 2, s12
	v_add_u32_e32 v64, v241, v219
	ds_read_b128 v[32:35], v64 offset:49152
	v_add_u32_e32 v66, v241, v215
	ds_read_b128 v[36:39], v66 offset:49152
	v_add_u32_e32 v67, v241, v186
	ds_read_b128 v[40:43], v67 offset:49152
	v_add_u32_e32 v73, v241, v233
	ds_read_b128 v[44:47], v73 offset:49152
	s_waitcnt lgkmcnt(3)
	v_mfma_f32_32x32x16_bf16 v[16:31], v[32:35], v[144:147], 0
	v_add_u32_e32 v76, v241, v234
	ds_read_b128 v[32:35], v76 offset:49152
	s_waitcnt lgkmcnt(3)
	v_mfma_f32_32x32x16_bf16 v[16:31], v[36:39], v[148:151], v[16:31]
	v_add_u32_e32 v77, v241, v235
	ds_read_b128 v[36:39], v77 offset:49152
	s_waitcnt lgkmcnt(3)
	v_mfma_f32_32x32x16_bf16 v[16:31], v[40:43], v[152:155], v[16:31]
	v_add_u32_e32 v78, v241, v236
	ds_read_b128 v[40:43], v78 offset:49152
	s_waitcnt lgkmcnt(3)
	v_mfma_f32_32x32x16_bf16 v[16:31], v[44:47], v[156:159], v[16:31]
	v_add_u32_e32 v79, v241, v237
	ds_read_b128 v[44:47], v79 offset:49152
	s_waitcnt lgkmcnt(3)
	v_mfma_f32_32x32x16_bf16 v[16:31], v[32:35], v[160:163], v[16:31]
	ds_read_b128 v[32:35], v64 offset:57344
	s_waitcnt lgkmcnt(3)
	v_mfma_f32_32x32x16_bf16 v[16:31], v[36:39], v[164:167], v[16:31]
	ds_read_b128 v[36:39], v66 offset:57344
	s_waitcnt lgkmcnt(3)
	v_mfma_f32_32x32x16_bf16 v[16:31], v[40:43], v[168:171], v[16:31]
	ds_read_b128 v[40:43], v67 offset:57344
	s_waitcnt lgkmcnt(3)
	v_mfma_f32_32x32x16_bf16 v[16:31], v[44:47], v[172:175], v[16:31]
	ds_read_b128 v[44:47], v73 offset:57344
	ds_read2_b32 v[48:49], v68 offset0:128 offset1:129
	ds_read2_b32 v[50:51], v68 offset0:130 offset1:131
	ds_read2_b32 v[52:53], v68 offset0:136 offset1:137
	ds_read2_b32 v[54:55], v68 offset0:138 offset1:139
	ds_read2_b32 v[56:57], v68 offset0:144 offset1:145
	ds_read2_b32 v[58:59], v68 offset0:146 offset1:147
	ds_read2_b32 v[60:61], v68 offset0:152 offset1:153
	ds_read2_b32 v[62:63], v68 offset0:154 offset1:155
	s_waitcnt lgkmcnt(11)
	v_mfma_f32_32x32x16_bf16 v[0:15], v[32:35], v[144:147], 0
	ds_read_b128 v[32:35], v76 offset:57344
	s_waitcnt lgkmcnt(11)
	v_mfma_f32_32x32x16_bf16 v[0:15], v[36:39], v[148:151], v[0:15]
	ds_read_b128 v[36:39], v77 offset:57344
	s_waitcnt lgkmcnt(11)
	v_mfma_f32_32x32x16_bf16 v[0:15], v[40:43], v[152:155], v[0:15]
	ds_read_b128 v[40:43], v78 offset:57344
	s_waitcnt lgkmcnt(11)
	v_mfma_f32_32x32x16_bf16 v[0:15], v[44:47], v[156:159], v[0:15]
	ds_read_b128 v[44:47], v79 offset:57344
	s_waitcnt lgkmcnt(3)
	v_mfma_f32_32x32x16_bf16 v[0:15], v[32:35], v[160:163], v[0:15]
	s_waitcnt lgkmcnt(2)
	v_mfma_f32_32x32x16_bf16 v[0:15], v[36:39], v[164:167], v[0:15]
	s_waitcnt lgkmcnt(1)
	v_mfma_f32_32x32x16_bf16 v[0:15], v[40:43], v[168:171], v[0:15]
	s_waitcnt lgkmcnt(0)
	v_mfma_f32_32x32x16_bf16 v[0:15], v[44:47], v[172:175], v[0:15]
	v_pk_fma_f32 v[16:17], v[16:17], s[94:95], v[48:49] op_sel_hi:[1,0,1]
	v_pk_fma_f32 v[18:19], v[18:19], s[94:95], v[50:51] op_sel_hi:[1,0,1]
	v_pk_fma_f32 v[20:21], v[20:21], s[94:95], v[52:53] op_sel_hi:[1,0,1]
	v_pk_fma_f32 v[22:23], v[22:23], s[94:95], v[54:55] op_sel_hi:[1,0,1]
	v_pk_fma_f32 v[24:25], v[24:25], s[94:95], v[56:57] op_sel_hi:[1,0,1]
	v_pk_fma_f32 v[26:27], v[26:27], s[94:95], v[58:59] op_sel_hi:[1,0,1]
	v_pk_fma_f32 v[28:29], v[28:29], s[94:95], v[60:61] op_sel_hi:[1,0,1]
	v_pk_fma_f32 v[30:31], v[30:31], s[94:95], v[62:63] op_sel_hi:[1,0,1]
	v_max_f32_e32 v70, v16, v17
	v_max3_f32 v70, v70, v18, v19
	v_max3_f32 v70, v70, v20, v21
	v_max3_f32 v70, v70, v22, v23
	v_max3_f32 v70, v70, v24, v25
	v_max3_f32 v70, v70, v26, v27
	v_max3_f32 v70, v70, v28, v29
	v_max3_f32 v70, v70, v30, v31
	ds_read2_b32 v[48:49], v68 offset0:160 offset1:161
	ds_read2_b32 v[50:51], v68 offset0:162 offset1:163
	ds_read2_b32 v[52:53], v68 offset0:168 offset1:169
	ds_read2_b32 v[54:55], v68 offset0:170 offset1:171
	ds_read2_b32 v[56:57], v68 offset0:176 offset1:177
	ds_read2_b32 v[58:59], v68 offset0:178 offset1:179
	ds_read2_b32 v[60:61], v68 offset0:184 offset1:185
	ds_read2_b32 v[62:63], v68 offset0:186 offset1:187
	ds_read_b64_tr_b16 v[32:33], v242 offset:0
	ds_read_b64_tr_b16 v[34:35], v242 offset:2048
	ds_read_b64_tr_b16 v[36:37], v242 offset:512
	ds_read_b64_tr_b16 v[38:39], v242 offset:2560
	ds_read_b64_tr_b16 v[40:41], v242 offset:4096
	ds_read_b64_tr_b16 v[42:43], v242 offset:6144
	s_waitcnt lgkmcnt(6)
	v_pk_fma_f32 v[0:1], v[0:1], s[94:95], v[48:49] op_sel_hi:[1,0,1]
	v_pk_fma_f32 v[2:3], v[2:3], s[94:95], v[50:51] op_sel_hi:[1,0,1]
	v_pk_fma_f32 v[4:5], v[4:5], s[94:95], v[52:53] op_sel_hi:[1,0,1]
	v_pk_fma_f32 v[6:7], v[6:7], s[94:95], v[54:55] op_sel_hi:[1,0,1]
	v_pk_fma_f32 v[8:9], v[8:9], s[94:95], v[56:57] op_sel_hi:[1,0,1]
	v_pk_fma_f32 v[10:11], v[10:11], s[94:95], v[58:59] op_sel_hi:[1,0,1]
	v_pk_fma_f32 v[12:13], v[12:13], s[94:95], v[60:61] op_sel_hi:[1,0,1]
	v_pk_fma_f32 v[14:15], v[14:15], s[94:95], v[62:63] op_sel_hi:[1,0,1]
	ds_read_b64_tr_b16 v[44:45], v242 offset:4608
	ds_read_b64_tr_b16 v[46:47], v242 offset:6656
	v_max3_f32 v70, v70, v0, v1
	v_max3_f32 v70, v70, v2, v3
	v_max3_f32 v70, v70, v4, v5
	v_max3_f32 v70, v70, v6, v7
	v_max3_f32 v70, v70, v8, v9
	v_max3_f32 v70, v70, v10, v11
	v_max3_f32 v70, v70, v12, v13
	v_max3_f32 v70, v70, v14, v15
	v_mov_b32_e32 v71, v70
	s_nop 1
	v_permlane32_swap_b32_e32 v70, v71
	v_max3_f32 v245, v243, v70, v71
	v_sub_f32_e32 v72, v245, v243
	v_cmp_lt_f32_e32 vcc, 0x41000000, v72
	s_cbranch_vccnz .Lft1_newmax
	v_mov_b32_e32 v245, v243

; __device__ __forceinline__ int crow(int r, int hi) { return (r & 3) + 8 * (r >> 2) + 4 * hi; }
; __device__ __forceinline__ void datt_stream(LAS unsigned char* lds, const DattRun& c, const float C, const int wv) {
;     ...
;         if (do0) {
; #pragma unroll
;             for (int r = 0; r < 16; ++r) { p0[r] = __builtin_amdgcn_exp2f(p0[r] - mn); ps += p0[r]; } }
;         if (do1) {
; #pragma unroll
;             for (int r = 0; r < 16; ++r) { p1[r] = __builtin_amdgcn_exp2f(p1[r] - mn); ps += p1[r]; } }
;         { auto rr = __builtin_amdgcn_permlane32_swap(__float_as_uint(ps), __float_as_uint(ps), false, false);
;           ps = __uint_as_float(rr[0]) + __uint_as_float(rr[1]); }
;         l_reg = l_reg * alpha + ps;
;         if (__any(alpha < 1.f)) { if (hi == 0) al_l[r32] = alpha; asm volatile("s_waitcnt lgkmcnt(0)" ::: "memory");
; #pragma unroll
;             for (int r = 0; r < 16; ++r) { const float a = al_l[crow(r, hi)];
; #pragma unroll
;                 for (int d = 0; d < 4; ++d) o[d][r] *= a; } }
;         const int vb = vb0 + b * SHM_T;
;     ...
;         if (do0) { bf16x8 pa0_, pa1_; DS_PK4(p0, 0, pa0_); DS_PK4(p0, 8, pa1_);
;             pv_half2<0, 1, 0>(o[0], o[1], vb, pa0_, pa1_); pv_half2<2, 3, 0>(o[2], o[3], vb, pa0_, pa1_); }
;         if (do1) { bf16x8 pa2_, pa3_; DS_PK4(p1, 0, pa2_); DS_PK4(p1, 8, pa3_);
;             pv_half2<0, 1, 1>(o[0], o[1], vb, pa2_, pa3_); pv_half2<2, 3, 1>(o[2], o[3], vb, pa2_, pa3_); }
.Lft1_noresc:
	v_permlane32_swap_b32_e32 v16, v18
	v_permlane32_swap_b32_e32 v17, v19
	v_permlane32_swap_b32_e32 v20, v22
	v_permlane32_swap_b32_e32 v21, v23
	v_pk_add_f32 v[0:1], v[0:1], v[70:71] neg_lo:[0,1] neg_hi:[0,1]
	v_pk_add_f32 v[2:3], v[2:3], v[70:71] neg_lo:[0,1] neg_hi:[0,1]
	v_pk_add_f32 v[4:5], v[4:5], v[70:71] neg_lo:[0,1] neg_hi:[0,1]
	v_pk_add_f32 v[6:7], v[6:7], v[70:71] neg_lo:[0,1] neg_hi:[0,1]
	v_pk_add_f32 v[8:9], v[8:9], v[70:71] neg_lo:[0,1] neg_hi:[0,1]
	v_pk_add_f32 v[10:11], v[10:11], v[70:71] neg_lo:[0,1] neg_hi:[0,1]
	v_pk_add_f32 v[12:13], v[12:13], v[70:71] neg_lo:[0,1] neg_hi:[0,1]
	v_pk_add_f32 v[14:15], v[14:15], v[70:71] neg_lo:[0,1] neg_hi:[0,1]
	v_exp_f32_e32 v0, v0
	v_exp_f32_e32 v1, v1
	v_exp_f32_e32 v2, v2
	v_exp_f32_e32 v3, v3
	v_exp_f32_e32 v4, v4
	v_exp_f32_e32 v5, v5
	v_exp_f32_e32 v6, v6
	v_exp_f32_e32 v7, v7
	v_exp_f32_e32 v8, v8
	v_exp_f32_e32 v9, v9
	v_exp_f32_e32 v10, v10
	v_exp_f32_e32 v11, v11
	v_exp_f32_e32 v12, v12
	v_exp_f32_e32 v13, v13
	v_exp_f32_e32 v14, v14
	v_exp_f32_e32 v15, v15
	v_pk_add_f32 v[74:75], v[74:75], v[0:1]
	v_pk_add_f32 v[74:75], v[74:75], v[2:3]
	v_pk_add_f32 v[74:75], v[74:75], v[4:5]
	v_pk_add_f32 v[74:75], v[74:75], v[6:7]
	v_pk_add_f32 v[74:75], v[74:75], v[8:9]
	v_pk_add_f32 v[74:75], v[74:75], v[10:11]
	v_pk_add_f32 v[74:75], v[74:75], v[12:13]
	v_pk_add_f32 v[74:75], v[74:75], v[14:15]
	v_add_f32_e32 v64, v74, v75
	s_waitcnt lgkmcnt(0)
	v_mfma_f32_32x32x16_bf16 v[80:95], v[16:19], v[32:35], v[80:95]
	ds_read_b64_tr_b16 v[32:33], v242 offset:8192
	ds_read_b64_tr_b16 v[34:35], v242 offset:10240
	v_mfma_f32_32x32x16_bf16 v[96:111], v[16:19], v[36:39], v[96:111]
	ds_read_b64_tr_b16 v[36:37], v242 offset:8704
	ds_read_b64_tr_b16 v[38:39], v242 offset:10752
	v_mfma_f32_32x32x16_bf16 v[80:95], v[20:23], v[40:43], v[80:95]
	ds_read_b64_tr_b16 v[40:41], v242 offset:12288
	ds_read_b64_tr_b16 v[42:43], v242 offset:14336
	v_mfma_f32_32x32x16_bf16 v[96:111], v[20:23], v[44:47], v[96:111]
	ds_read_b64_tr_b16 v[44:45], v242 offset:12800
	ds_read_b64_tr_b16 v[46:47], v242 offset:14848
	v_mfma_f32_32x32x16_bf16 v[112:127], v[16:19], v[48:51], v[112:127]
	ds_read_b64_tr_b16 v[48:49], v242 offset:9216
	ds_read_b64_tr_b16 v[50:51], v242 offset:11264
	v_mfma_f32_32x32x16_bf16 v[128:143], v[16:19], v[52:55], v[128:143]
	ds_read_b64_tr_b16 v[52:53], v242 offset:9728
	ds_read_b64_tr_b16 v[54:55], v242 offset:11776
	v_mfma_f32_32x32x16_bf16 v[112:127], v[20:23], v[56:59], v[112:127]
	ds_read_b64_tr_b16 v[56:57], v242 offset:13312
	ds_read_b64_tr_b16 v[58:59], v242 offset:15360
	v_mfma_f32_32x32x16_bf16 v[128:143], v[20:23], v[60:63], v[128:143]
	ds_read_b64_tr_b16 v[60:61], v242 offset:13824
	s_waitcnt lgkmcnt(14)
	ds_read_b64_tr_b16 v[62:63], v242 offset:15872
	v_cvt_pk_bf16_f32 v0, v0, v1
	v_cvt_pk_bf16_f32 v1, v2, v3
	v_cvt_pk_bf16_f32 v2, v4, v5
	v_cvt_pk_bf16_f32 v3, v6, v7
	v_cvt_pk_bf16_f32 v4, v8, v9
	v_cvt_pk_bf16_f32 v5, v10, v11
	v_cvt_pk_bf16_f32 v6, v12, v13
	v_cvt_pk_bf16_f32 v7, v14, v15
	v_mov_b32_e32 v67, v64
	v_permlane32_swap_b32_e32 v0, v2
	v_permlane32_swap_b32_e32 v1, v3
	v_permlane32_swap_b32_e32 v4, v6
	v_permlane32_swap_b32_e32 v5, v7
	v_permlane32_swap_b32_e32 v64, v67
	s_waitcnt lgkmcnt(14)
	v_mfma_f32_32x32x16_bf16 v[80:95], v[0:3], v[32:35], v[80:95]
	s_waitcnt lgkmcnt(12)
	v_mfma_f32_32x32x16_bf16 v[96:111], v[0:3], v[36:39], v[96:111]
	s_waitcnt lgkmcnt(10)
	v_mfma_f32_32x32x16_bf16 v[80:95], v[4:7], v[40:43], v[80:95]
	s_waitcnt lgkmcnt(8)
	v_mfma_f32_32x32x16_bf16 v[96:111], v[4:7], v[44:47], v[96:111]
	s_waitcnt lgkmcnt(6)
	v_mfma_f32_32x32x16_bf16 v[112:127], v[0:3], v[48:51], v[112:127]
	s_waitcnt lgkmcnt(4)
	v_mfma_f32_32x32x16_bf16 v[128:143], v[0:3], v[52:55], v[128:143]
	s_waitcnt lgkmcnt(2)
	v_mfma_f32_32x32x16_bf16 v[112:127], v[4:7], v[56:59], v[112:127]
	s_waitcnt lgkmcnt(0)
	v_mfma_f32_32x32x16_bf16 v[128:143], v[4:7], v[60:63], v[128:143]
	s_nop 1
	s_branch .LBB0_519

; #define LAS __attribute__((address_space(3)))
; __device__ __forceinline__ bf16 f2bf(float f) { return (bf16)cvt_pk_bf16(f, f); }
; template <int PH, bool PRB = false>
; __device__ __forceinline__ void run_phase(int layer, LAS unsigned char* lds, const int wv_) {
;     ...
;             u32x4 vw[4];
; #pragma unroll
;             for (int it = 0; it < 4; ++it) { const int item = tid + NT * it; vw[it] = *(const u32x4*)(z + (size_t)(t0 + (item & 127)) * EVEN_IN + 512 + g * 128 + 8 * (item >> 7)); }
; #pragma unroll
;             for (int it = 0; it < 4; ++it) {
;                 const int item = tid + NT * it, q = item & 127, cc = item >> 7;
;                 const u32x4 w = vw[it]; const float mu = st[2 * q], rstd = st[2 * q + 1];
; #pragma unroll
;                 for (int k = 0; k < 8; ++k) { const int c = 8 * cc + k; const float v = (k & 1) ? __uint_as_float(w[k >> 1] & 0xffff0000u) : __uint_as_float(w[k >> 1] << 16);
;                     *(LAS bf16*)(vnt + c * 272 + q * 2) = f2bf((v - mu) * rstd * lg[g * 128 + c] + lb[g * 128 + c]); }
;             }
.LBB0_639:
	s_or_b64 exec, exec, s[12:13]
	s_waitcnt lgkmcnt(0)
	v_or_b32_e32 v2, s18, v116
	v_mov_b64_e32 v[0:1], s[2:3]
	v_mad_i64_i32 v[0:1], s[4:5], v2, s60, v[0:1]
	s_lshl_b32 s50, s19, 1
	v_lshl_add_u64 v[0:1], v[0:1], 0, s[50:51]
	v_lshl_add_u64 v[2:3], v[62:63], 1, v[0:1]
	s_barrier
	global_load_dwordx4 v[12:15], v[2:3], off offset:1024
	v_add_u32_e32 v2, s19, v62
	v_ashrrev_i32_e32 v3, 31, v2
	v_lshlrev_b64 v[2:3], 2, v[2:3]
	v_lshl_add_u64 v[20:21], s[6:7], 0, v[2:3]
	v_lshl_add_u64 v[22:23], s[8:9], 0, v[2:3]
	global_load_dword v26, v[20:21], off
	global_load_dword v27, v[22:23], off
	ds_read_b64 v[24:25], v117
	v_lshl_add_u64 v[2:3], v[66:67], 1, v[0:1]
	v_lshl_add_u64 v[4:5], v[68:69], 1, v[0:1]
	v_lshl_add_u64 v[0:1], v[70:71], 1, v[0:1]
	global_load_dwordx4 v[8:11], v[2:3], off offset:1024
	s_nop 0
	global_load_dwordx4 v[4:7], v[4:5], off offset:1024
	s_nop 0
	global_load_dwordx4 v[0:3], v[0:1], off offset:1024
	global_load_dwordx4 v[188:191], v[20:21], off
	global_load_dwordx4 v[196:199], v[22:23], off
	global_load_dwordx4 v[192:195], v[20:21], off offset:16
	global_load_dwordx4 v[200:203], v[22:23], off offset:16
	global_load_dwordx4 v[204:207], v[20:21], off offset:128
	global_load_dwordx4 v[212:215], v[22:23], off offset:128
	global_load_dwordx4 v[208:211], v[20:21], off offset:144
	global_load_dwordx4 v[222:225], v[22:23], off offset:144
	global_load_dwordx4 v[230:233], v[20:21], off offset:256
	global_load_dwordx4 v[238:241], v[22:23], off offset:256
	global_load_dwordx4 v[234:237], v[20:21], off offset:272
	global_load_dwordx4 v[246:249], v[22:23], off offset:272
	s_waitcnt vmcnt(0) lgkmcnt(0)
	v_lshlrev_b32_e32 v216, 16, v12
	v_sub_f32_e32 v216, v216, v24
	v_mul_f32_e32 v216, v25, v216
	v_fmac_f32_e32 v196, v188, v216
	v_cvt_pk_bf16_f32 v196, v196, v196
	ds_write_b16 v141, v196
	v_and_b32_e32 v217, 0xffff0000, v12
	v_sub_f32_e32 v217, v217, v24
	v_mul_f32_e32 v217, v25, v217
	v_fmac_f32_e32 v197, v189, v217
	v_cvt_pk_bf16_f32 v197, v197, v197
	ds_write_b16 v141, v197 offset:272
	v_lshlrev_b32_e32 v216, 16, v13
	v_sub_f32_e32 v216, v216, v24
	v_mul_f32_e32 v216, v25, v216
	v_fmac_f32_e32 v198, v190, v216
	v_cvt_pk_bf16_f32 v198, v198, v198
	ds_write_b16 v141, v198 offset:544
	v_and_b32_e32 v217, 0xffff0000, v13
	v_sub_f32_e32 v217, v217, v24
	v_mul_f32_e32 v217, v25, v217
	v_fmac_f32_e32 v199, v191, v217
	v_cvt_pk_bf16_f32 v199, v199, v199
	ds_write_b16 v141, v199 offset:816
	v_lshlrev_b32_e32 v216, 16, v14
	v_sub_f32_e32 v216, v216, v24
	v_mul_f32_e32 v216, v25, v216
	v_fmac_f32_e32 v200, v192, v216
	v_cvt_pk_bf16_f32 v200, v200, v200
	ds_write_b16 v141, v200 offset:1088
	v_and_b32_e32 v217, 0xffff0000, v14
	v_sub_f32_e32 v217, v217, v24
	v_mul_f32_e32 v217, v25, v217
	v_fmac_f32_e32 v201, v193, v217
	v_cvt_pk_bf16_f32 v201, v201, v201
	ds_write_b16 v141, v201 offset:1360
	v_lshlrev_b32_e32 v216, 16, v15
	v_sub_f32_e32 v216, v216, v24
	v_mul_f32_e32 v216, v25, v216
	v_fmac_f32_e32 v202, v194, v216
	v_cvt_pk_bf16_f32 v202, v202, v202
	ds_write_b16 v141, v202 offset:1632
	v_and_b32_e32 v217, 0xffff0000, v15
	v_sub_f32_e32 v217, v217, v24
	v_mul_f32_e32 v217, v25, v217
	v_fmac_f32_e32 v203, v195, v217
	v_cvt_pk_bf16_f32 v203, v203, v203
	ds_write_b16 v142, v203
	global_load_dwordx4 v[188:191], v[20:21], off offset:384
	global_load_dwordx4 v[196:199], v[22:23], off offset:384
	global_load_dwordx4 v[192:195], v[20:21], off offset:400
	global_load_dwordx4 v[200:203], v[22:23], off offset:400
	v_lshlrev_b32_e32 v216, 16, v8
	v_sub_f32_e32 v216, v216, v24
	v_mul_f32_e32 v216, v25, v216
	v_fmac_f32_e32 v212, v204, v216
	v_cvt_pk_bf16_f32 v212, v212, v212
	ds_write_b16 v143, v212
	v_and_b32_e32 v217, 0xffff0000, v8
	v_sub_f32_e32 v217, v217, v24
	v_mul_f32_e32 v217, v25, v217
	v_fmac_f32_e32 v213, v205, v217
	v_cvt_pk_bf16_f32 v213, v213, v213
	ds_write_b16 v143, v213 offset:272
	v_lshlrev_b32_e32 v216, 16, v9
	v_sub_f32_e32 v216, v216, v24
	v_mul_f32_e32 v216, v25, v216
	v_fmac_f32_e32 v214, v206, v216
	v_cvt_pk_bf16_f32 v214, v214, v214
	ds_write_b16 v143, v214 offset:544
	v_and_b32_e32 v217, 0xffff0000, v9
	v_sub_f32_e32 v217, v217, v24
	v_mul_f32_e32 v217, v25, v217
	v_fmac_f32_e32 v215, v207, v217
	v_cvt_pk_bf16_f32 v215, v215, v215
	ds_write_b16 v143, v215 offset:816
	v_lshlrev_b32_e32 v216, 16, v10
	v_sub_f32_e32 v216, v216, v24
	v_mul_f32_e32 v216, v25, v216
	v_fmac_f32_e32 v222, v208, v216
	v_cvt_pk_bf16_f32 v222, v222, v222
	ds_write_b16 v143, v222 offset:1088
	v_and_b32_e32 v217, 0xffff0000, v10
	v_sub_f32_e32 v217, v217, v24
	v_mul_f32_e32 v217, v25, v217
	v_fmac_f32_e32 v223, v209, v217
	v_cvt_pk_bf16_f32 v223, v223, v223
	ds_write_b16 v143, v223 offset:1360
	v_lshlrev_b32_e32 v216, 16, v11
	v_sub_f32_e32 v216, v216, v24
	v_mul_f32_e32 v216, v25, v216
	v_fmac_f32_e32 v224, v210, v216
	v_cvt_pk_bf16_f32 v224, v224, v224
	ds_write_b16 v143, v224 offset:1632
	v_and_b32_e32 v217, 0xffff0000, v11
	v_sub_f32_e32 v217, v217, v24
	v_mul_f32_e32 v217, v25, v217
	v_fmac_f32_e32 v225, v211, v217
	v_cvt_pk_bf16_f32 v225, v225, v225
	ds_write_b16 v144, v225
	v_lshlrev_b32_e32 v216, 16, v4
	v_sub_f32_e32 v216, v216, v24
	v_mul_f32_e32 v216, v25, v216
	v_fmac_f32_e32 v238, v230, v216
	v_cvt_pk_bf16_f32 v238, v238, v238
	ds_write_b16 v145, v238
	v_and_b32_e32 v217, 0xffff0000, v4
	v_sub_f32_e32 v217, v217, v24
	v_mul_f32_e32 v217, v25, v217
	v_fmac_f32_e32 v239, v231, v217
	v_cvt_pk_bf16_f32 v239, v239, v239
	ds_write_b16 v145, v239 offset:272
	v_lshlrev_b32_e32 v216, 16, v5
	v_sub_f32_e32 v216, v216, v24
	v_mul_f32_e32 v216, v25, v216
	v_fmac_f32_e32 v240, v232, v216
	v_cvt_pk_bf16_f32 v240, v240, v240
	ds_write_b16 v145, v240 offset:544
	v_and_b32_e32 v217, 0xffff0000, v5
	v_sub_f32_e32 v217, v217, v24
	v_mul_f32_e32 v217, v25, v217
	v_fmac_f32_e32 v241, v233, v217
	v_cvt_pk_bf16_f32 v241, v241, v241
	ds_write_b16 v145, v241 offset:816
	v_lshlrev_b32_e32 v216, 16, v6
	v_sub_f32_e32 v216, v216, v24
	v_mul_f32_e32 v216, v25, v216
	v_fmac_f32_e32 v246, v234, v216
	v_cvt_pk_bf16_f32 v246, v246, v246
	ds_write_b16 v145, v246 offset:1088
	v_and_b32_e32 v217, 0xffff0000, v6
	v_sub_f32_e32 v217, v217, v24
	v_mul_f32_e32 v217, v25, v217
	v_fmac_f32_e32 v247, v235, v217
	v_cvt_pk_bf16_f32 v247, v247, v247
	ds_write_b16 v145, v247 offset:1360
	v_lshlrev_b32_e32 v216, 16, v7
	v_sub_f32_e32 v216, v216, v24
	v_mul_f32_e32 v216, v25, v216
	v_fmac_f32_e32 v248, v236, v216
	v_cvt_pk_bf16_f32 v248, v248, v248
	ds_write_b16 v145, v248 offset:1632
	v_and_b32_e32 v217, 0xffff0000, v7
	v_sub_f32_e32 v217, v217, v24
	v_mul_f32_e32 v217, v25, v217
	v_fmac_f32_e32 v249, v237, v217
	v_cvt_pk_bf16_f32 v249, v249, v249
	ds_write_b16 v146, v249
	s_waitcnt vmcnt(0)
; #define LAS __attribute__((address_space(3)))
; __device__ __forceinline__ bf16 f2bf(float f) { return (bf16)cvt_pk_bf16(f, f); }
; __device__ __forceinline__ int crow(int r, int hi) { return (r & 3) + 8 * (r >> 2) + 4 * hi; }
; template <int PH, bool PRB = false>
; __device__ __forceinline__ void run_phase(int layer, LAS unsigned char* lds, const int wv_) {
;     ...
;             for (int it = 0; it < 4; ++it) {
;                 const int item = tid + NT * it, q = item & 127, cc = item >> 7;
;                 const u32x4 w = vw[it]; const float mu = st[2 * q], rstd = st[2 * q + 1];
; #pragma unroll
;                 for (int k = 0; k < 8; ++k) { const int c = 8 * cc + k; const float v = (k & 1) ? __uint_as_float(w[k >> 1] & 0xffff0000u) : __uint_as_float(w[k >> 1] << 16);
;                     *(LAS bf16*)(vnt + c * 272 + q * 2) = f2bf((v - mu) * rstd * lg[g * 128 + c] + lb[g * 128 + c]); }
;             }
;     ...
;                 const int col = g * 128 + 32 * cb0 + r32; bf16 u0[16], u1[16]; float bias[16];
; #pragma unroll
;                 for (int r = 0; r < 16; ++r) { const int prow = 32 * pb + att::crow(r, hi), tok = t0 + prow; bias[r] = bs[g * 128 + prow];
;                     u0[r] = z[(size_t)tok * EVEN_IN + col]; u1[r] = z[(size_t)tok * EVEN_IN + col + 32]; }
; #pragma unroll
;                 for (int r = 0; r < 16; ++r) { const int tok = t0 + 32 * pb + att::crow(r, hi);
	v_lshlrev_b32_e32 v216, 16, v0
	v_sub_f32_e32 v216, v216, v24
	v_mul_f32_e32 v216, v25, v216
	v_fmac_f32_e32 v196, v188, v216
	v_cvt_pk_bf16_f32 v196, v196, v196
	ds_write_b16 v147, v196
	v_and_b32_e32 v217, 0xffff0000, v0
	v_sub_f32_e32 v217, v217, v24
	v_mul_f32_e32 v217, v25, v217
	v_fmac_f32_e32 v197, v189, v217
	v_cvt_pk_bf16_f32 v197, v197, v197
	ds_write_b16 v147, v197 offset:272
	v_lshlrev_b32_e32 v216, 16, v1
	v_sub_f32_e32 v216, v216, v24
	v_mul_f32_e32 v216, v25, v216
	v_fmac_f32_e32 v198, v190, v216
	v_cvt_pk_bf16_f32 v198, v198, v198
	ds_write_b16 v147, v198 offset:544
	v_and_b32_e32 v217, 0xffff0000, v1
	v_sub_f32_e32 v217, v217, v24
	v_mul_f32_e32 v217, v25, v217
	v_fmac_f32_e32 v199, v191, v217
	v_cvt_pk_bf16_f32 v199, v199, v199
	ds_write_b16 v147, v199 offset:816
	v_lshlrev_b32_e32 v216, 16, v2
	v_sub_f32_e32 v216, v216, v24
	v_mul_f32_e32 v216, v25, v216
	v_fmac_f32_e32 v200, v192, v216
	v_cvt_pk_bf16_f32 v200, v200, v200
	ds_write_b16 v147, v200 offset:1088
	v_and_b32_e32 v217, 0xffff0000, v2
	v_sub_f32_e32 v217, v217, v24
	v_mul_f32_e32 v217, v25, v217
	v_fmac_f32_e32 v201, v193, v217
	v_cvt_pk_bf16_f32 v201, v201, v201
	ds_write_b16 v147, v201 offset:1360
	v_lshlrev_b32_e32 v216, 16, v3
	v_sub_f32_e32 v216, v216, v24
	v_mul_f32_e32 v216, v25, v216
	v_fmac_f32_e32 v202, v194, v216
	v_cvt_pk_bf16_f32 v202, v202, v202
	ds_write_b16 v147, v202 offset:1632
	v_and_b32_e32 v217, 0xffff0000, v3
	v_sub_f32_e32 v217, v217, v24
	v_mul_f32_e32 v217, v25, v217
	v_fmac_f32_e32 v203, v195, v217
	v_cvt_pk_bf16_f32 v203, v203, v203
	ds_write_b16 v148, v203
	s_and_b32 s4, s14, 0x7fffffc
	s_add_i32 s4, s4, s15
	v_lshl_or_b32 v96, s4, 5, v119
	v_add_u32_e32 v29, s18, v139
	v_readlane_b32 s5, v254, 20
	v_ashrrev_i32_e32 v97, 31, v96
	s_add_i32 s16, s16, s5
	v_or_b32_e32 v110, 1, v96
	v_or_b32_e32 v112, 2, v96
	v_or_b32_e32 v150, 3, v96
	v_or_b32_e32 v152, 8, v96
	v_or_b32_e32 v160, 9, v96
	v_or_b32_e32 v162, 10, v96
	v_or_b32_e32 v164, 11, v96
	v_or_b32_e32 v166, 16, v96
	v_or_b32_e32 v168, 17, v96
	v_or_b32_e32 v170, 18, v96
	v_or_b32_e32 v172, 19, v96
	v_or_b32_e32 v174, 24, v96
	v_or_b32_e32 v176, 25, v96
	v_or_b32_e32 v178, 26, v96
	v_or_b32_e32 v106, 27, v96
	v_lshlrev_b64 v[180:181], 11, v[96:97]
	v_ashrrev_i32_e32 v151, 31, v150
	v_ashrrev_i32_e32 v153, 31, v152
	v_lshlrev_b64 v[184:185], 11, v[150:151]
	v_lshlrev_b64 v[186:187], 11, v[152:153]
	v_ashrrev_i32_e32 v111, 31, v110
	v_ashrrev_i32_e32 v161, 31, v160
	v_ashrrev_i32_e32 v163, 31, v162
	v_ashrrev_i32_e32 v165, 31, v164
	v_ashrrev_i32_e32 v167, 31, v166
	v_ashrrev_i32_e32 v113, 31, v112
	v_ashrrev_i32_e32 v169, 31, v168
	v_lshlrev_b64 v[182:183], 11, v[112:113]
	v_lshlrev_b64 v[112:113], 11, v[168:169]
	v_ashrrev_i32_e32 v171, 31, v170
	v_ashrrev_i32_e32 v173, 31, v172
	v_ashrrev_i32_e32 v107, 31, v106
	v_ashrrev_i32_e32 v175, 31, v174
	v_ashrrev_i32_e32 v177, 31, v176
	v_ashrrev_i32_e32 v179, 31, v178
	s_add_i32 s14, s14, s95
	s_add_i32 s17, s17, s81
	s_cmpk_lt_i32 s14, 0x200
	v_add_u32_e32 v28, s18, v138
	v_add_u32_e32 v12, s19, v121
	v_add_u32_e32 v27, s18, v137
	s_nop 0
	v_ashrrev_i32_e32 v13, 31, v12
	v_lshlrev_b64 v[12:13], 2, v[12:13]
	v_lshl_add_u64 v[20:21], s[6:7], 0, v[12:13]
	v_lshl_add_u64 v[12:13], s[8:9], 0, v[12:13]
	v_add_u32_e32 v12, s19, v66
	v_ashrrev_i32_e32 v13, 31, v12
	v_lshlrev_b64 v[12:13], 2, v[12:13]
	v_lshl_add_u64 v[20:21], s[6:7], 0, v[12:13]
	v_lshl_add_u64 v[12:13], s[8:9], 0, v[12:13]
	v_add_u32_e32 v26, s18, v136
	ds_read_b64 v[14:15], v117
	v_add_u32_e32 v25, s18, v135
	v_add_u32_e32 v24, s18, v134
	v_add_u32_e32 v8, s19, v122
	v_add_u32_e32 v23, s18, v133
	s_nop 0
	v_ashrrev_i32_e32 v9, 31, v8
	v_lshlrev_b64 v[8:9], 2, v[8:9]
	v_lshl_add_u64 v[12:13], s[6:7], 0, v[8:9]
	v_lshl_add_u64 v[8:9], s[8:9], 0, v[8:9]
	v_add_u32_e32 v8, s19, v68
	v_ashrrev_i32_e32 v9, 31, v8
	v_lshlrev_b64 v[8:9], 2, v[8:9]
	v_lshl_add_u64 v[12:13], s[6:7], 0, v[8:9]
	v_lshl_add_u64 v[8:9], s[8:9], 0, v[8:9]
	v_add_u32_e32 v22, s18, v132
	ds_read_b64 v[10:11], v117
	v_add_u32_e32 v21, s18, v131
	v_add_u32_e32 v20, s18, v130
	v_add_u32_e32 v4, s19, v123
	s_nop 0
	v_ashrrev_i32_e32 v5, 31, v4
	v_lshlrev_b64 v[4:5], 2, v[4:5]
	v_lshl_add_u64 v[8:9], s[6:7], 0, v[4:5]
	v_lshl_add_u64 v[4:5], s[8:9], 0, v[4:5]
	v_add_u32_e32 v4, s19, v70
	v_ashrrev_i32_e32 v5, 31, v4
	v_lshlrev_b64 v[4:5], 2, v[4:5]
	v_lshl_add_u64 v[8:9], s[6:7], 0, v[4:5]
	v_lshl_add_u64 v[12:13], s[8:9], 0, v[4:5]
	ds_read_b64 v[4:5], v117
	v_add_u32_e32 v14, s18, v128
	v_add_u32_e32 v15, s18, v129
	v_add_u32_e32 v11, s18, v125
	v_add_u32_e32 v0, s19, v124
	s_nop 0
	v_ashrrev_i32_e32 v1, 31, v0
	v_lshlrev_b64 v[0:1], 2, v[0:1]
	v_lshl_add_u64 v[6:7], s[6:7], 0, v[0:1]
	v_lshl_add_u64 v[0:1], s[8:9], 0, v[0:1]
	v_add_u32_e32 v12, s18, v126
	v_add_u32_e32 v13, s18, v127
	v_or_b32_e32 v1, s19, v118
	v_add_u32_e32 v0, s19, v120
	v_lshlrev_b32_e32 v64, 1, v1
	v_ashrrev_i32_e32 v1, 31, v0
	v_lshl_add_u64 v[78:79], v[0:1], 2, s[10:11]
	v_add_u32_e32 v10, s18, v120
	v_lshl_add_u64 v[6:7], s[2:3], 0, v[64:65]
	v_mad_i64_i32 v[154:155], s[4:5], v10, s60, v[6:7]
	v_mad_i64_i32 v[156:157], s[4:5], v11, s60, v[6:7]
	v_mad_i64_i32 v[158:159], s[4:5], v12, s60, v[6:7]
	v_mad_i64_i32 v[108:109], s[4:5], v13, s60, v[6:7]
	v_mad_i64_i32 v[104:105], s[4:5], v14, s60, v[6:7]
	v_mad_i64_i32 v[102:103], s[4:5], v15, s60, v[6:7]
	v_mad_i64_i32 v[100:101], s[4:5], v20, s60, v[6:7]
	v_mad_i64_i32 v[94:95], s[4:5], v21, s60, v[6:7]
	v_mad_i64_i32 v[92:93], s[4:5], v22, s60, v[6:7]
	v_mad_i64_i32 v[90:91], s[4:5], v23, s60, v[6:7]
	v_mad_i64_i32 v[88:89], s[4:5], v24, s60, v[6:7]
	v_mad_i64_i32 v[86:87], s[4:5], v25, s60, v[6:7]
	v_mad_i64_i32 v[84:85], s[4:5], v26, s60, v[6:7]
	v_mad_i64_i32 v[82:83], s[4:5], v27, s60, v[6:7]
	v_mad_i64_i32 v[80:81], s[4:5], v28, s60, v[6:7]
	v_mad_i64_i32 v[76:77], s[4:5], v29, s60, v[6:7]
	v_lshl_add_u64 v[74:75], s[0:1], 0, v[64:65]
	s_waitcnt lgkmcnt(0)
	s_barrier
; #define LAS __attribute__((address_space(3)))
; __device__ __forceinline__ int crow(int r, int hi) { return (r & 3) + 8 * (r >> 2) + 4 * hi; }
; template <int PH, bool PRB = false>
; __device__ __forceinline__ void run_phase(int layer, LAS unsigned char* lds, const int wv_) {
;     ...
;             f32x16 acc0, acc1;
; #pragma unroll
;             for (int r = 0; r < 16; ++r) { acc0[r] = 0.f; acc1[r] = 0.f; }
; #pragma unroll
;             for (int ks = 0; ks < 8; ++ks) {
;                 const bf16x8 b0 = *(const LAS bf16x8*)(vnt + (32 * cb0 + r32) * 272 + (16 * ks + 8 * hi) * 2);
;                 const bf16x8 b1 = *(const LAS bf16x8*)(vnt + (32 * (cb0 + 1) + r32) * 272 + (16 * ks + 8 * hi) * 2);
;                 acc0 = __builtin_amdgcn_mfma_f32_32x32x16_bf16(af[ks], b0, acc0, 0, 0, 0);
;                 acc1 = __builtin_amdgcn_mfma_f32_32x32x16_bf16(af[ks], b1, acc1, 0, 0, 0);
;             }
;             {
;                 const int col = g * 128 + 32 * cb0 + r32; bf16 u0[16], u1[16]; float bias[16];
; #pragma unroll
;                 for (int r = 0; r < 16; ++r) { const int prow = 32 * pb + att::crow(r, hi), tok = t0 + prow; bias[r] = bs[g * 128 + prow];
;                     u0[r] = z[(size_t)tok * EVEN_IN + col]; u1[r] = z[(size_t)tok * EVEN_IN + col + 32]; }
	ds_read_b128 v[0:3], v149
	ds_read_b128 v[96:99], v149 offset:32
	s_waitcnt lgkmcnt(1)
	v_mfma_f32_32x32x16_bf16 v[0:15], v[16:19], v[0:3], 0
	ds_read_b128 v[20:23], v149 offset:8704
	ds_read_b128 v[150:153], v149 offset:96
	s_waitcnt lgkmcnt(2)
	v_mfma_f32_32x32x16_bf16 v[0:15], v[56:59], v[96:99], v[0:15]
	ds_read_b128 v[96:99], v149 offset:8736
	s_waitcnt lgkmcnt(2)
	v_mfma_f32_32x32x16_bf16 v[16:31], v[16:19], v[20:23], 0
	s_waitcnt lgkmcnt(0)
	v_mfma_f32_32x32x16_bf16 v[16:31], v[56:59], v[96:99], v[16:31]
	ds_read_b128 v[96:99], v149 offset:64
	v_lshl_add_u64 v[56:57], v[74:75], 0, v[180:181]
	v_lshlrev_b64 v[180:181], 11, v[110:111]
	v_lshlrev_b64 v[110:111], 11, v[160:161]
	v_lshlrev_b64 v[58:59], 11, v[162:163]
	s_waitcnt lgkmcnt(0)
	v_mfma_f32_32x32x16_bf16 v[0:15], v[52:55], v[96:99], v[0:15]
	ds_read_b128 v[96:99], v149 offset:8768
	s_waitcnt lgkmcnt(0)
	v_mfma_f32_32x32x16_bf16 v[16:31], v[52:55], v[96:99], v[16:31]
	global_load_ushort v64, v[154:155], off
	global_load_dwordx4 v[52:55], v[78:79], off
	global_load_ushort v160, v[154:155], off offset:64
	global_load_ushort v161, v[156:157], off
	global_load_ushort v162, v[156:157], off offset:64
	global_load_ushort v163, v[158:159], off
	v_lshlrev_b64 v[96:97], 11, v[164:165]
	v_lshlrev_b64 v[98:99], 11, v[166:167]
	global_load_ushort v164, v[158:159], off offset:64
	v_mfma_f32_32x32x16_bf16 v[0:15], v[48:51], v[150:153], v[0:15]
	ds_read_b128 v[150:153], v149 offset:8800
	global_load_ushort v165, v[108:109], off
	global_load_ushort v166, v[108:109], off offset:64
	v_lshlrev_b64 v[154:155], 11, v[170:171]
	v_lshlrev_b64 v[156:157], 11, v[172:173]
	v_lshlrev_b64 v[108:109], 11, v[174:175]
	v_lshlrev_b64 v[158:159], 11, v[178:179]
	s_waitcnt lgkmcnt(0)
	v_mfma_f32_32x32x16_bf16 v[16:31], v[48:51], v[150:153], v[16:31]
	ds_read_b128 v[150:153], v149 offset:128
	global_load_ushort v167, v[104:105], off
	global_load_dwordx4 v[48:51], v[78:79], off offset:32
	global_load_ushort v168, v[104:105], off offset:64
	global_load_ushort v169, v[102:103], off
	global_load_ushort v170, v[102:103], off offset:64
	global_load_ushort v171, v[100:101], off
	global_load_ushort v172, v[100:101], off offset:64
	v_lshlrev_b64 v[104:105], 11, v[176:177]
	s_waitcnt lgkmcnt(0)
	v_mfma_f32_32x32x16_bf16 v[0:15], v[44:47], v[150:153], v[0:15]
	ds_read_b128 v[150:153], v149 offset:8832
	s_waitcnt lgkmcnt(0)
	v_mfma_f32_32x32x16_bf16 v[16:31], v[44:47], v[150:153], v[16:31]
	global_load_ushort v150, v[94:95], off
	global_load_ushort v151, v[94:95], off offset:64
	ds_read_b128 v[44:47], v149 offset:160
	v_lshlrev_b64 v[94:95], 11, v[106:107]
	global_load_ushort v106, v[92:93], off
	global_load_dwordx4 v[100:103], v[78:79], off offset:64
	global_load_ushort v107, v[92:93], off offset:64
	global_load_ushort v152, v[90:91], off
	global_load_ushort v153, v[90:91], off offset:64
	global_load_ushort v173, v[88:89], off
	global_load_ushort v174, v[88:89], off offset:64
	s_waitcnt lgkmcnt(0)
	v_mfma_f32_32x32x16_bf16 v[0:15], v[40:43], v[44:47], v[0:15]
	ds_read_b128 v[44:47], v149 offset:8864
	global_load_ushort v175, v[86:87], off
	global_load_ushort v176, v[86:87], off offset:64
	v_lshl_add_u64 v[90:91], v[74:75], 0, v[180:181]
	v_lshl_add_u64 v[92:93], v[74:75], 0, v[182:183]
	v_lshl_add_u64 v[86:87], v[74:75], 0, v[184:185]
	v_lshl_add_u64 v[88:89], v[74:75], 0, v[108:109]
	s_waitcnt lgkmcnt(0)
	v_mfma_f32_32x32x16_bf16 v[16:31], v[40:43], v[44:47], v[16:31]
	ds_read_b128 v[40:43], v149 offset:192
	global_load_ushort v177, v[84:85], off
	global_load_dwordx4 v[44:47], v[78:79], off offset:96
	global_load_ushort v178, v[84:85], off offset:64
	global_load_ushort v179, v[82:83], off
	global_load_ushort v180, v[82:83], off offset:64
	global_load_ushort v181, v[80:81], off
	v_lshl_add_u64 v[82:83], v[74:75], 0, v[110:111]
	global_load_ushort v110, v[80:81], off offset:64
	global_load_ushort v111, v[76:77], off
	global_load_ushort v182, v[76:77], off offset:64
	s_waitcnt lgkmcnt(0)
	v_mfma_f32_32x32x16_bf16 v[0:15], v[36:39], v[40:43], v[0:15]
	ds_read_b128 v[40:43], v149 offset:8896
	v_lshl_add_u64 v[78:79], v[74:75], 0, v[186:187]
	v_lshl_add_u64 v[76:77], v[74:75], 0, v[112:113]
	v_lshl_add_u64 v[80:81], v[74:75], 0, v[154:155]
	v_lshl_add_u64 v[84:85], v[74:75], 0, v[156:157]
	s_waitcnt vmcnt(2)
	v_lshlrev_b32_e32 v108, 16, v110
	s_waitcnt lgkmcnt(0)
	v_mfma_f32_32x32x16_bf16 v[16:31], v[36:39], v[40:43], v[16:31]
	ds_read_b128 v[36:39], v149 offset:224
	v_lshl_add_u64 v[40:41], v[74:75], 0, v[58:59]
	v_lshl_add_u64 v[42:43], v[74:75], 0, v[96:97]
	v_lshl_add_u64 v[58:59], v[74:75], 0, v[98:99]
	v_lshl_add_u64 v[96:97], v[74:75], 0, v[104:105]
	v_lshl_add_u64 v[98:99], v[74:75], 0, v[158:159]
	v_lshl_add_u64 v[74:75], v[74:75], 0, v[94:95]
	s_waitcnt lgkmcnt(0)
	v_mfma_f32_32x32x16_bf16 v[0:15], v[32:35], v[36:39], v[0:15]
	ds_read_b128 v[36:39], v149 offset:8928
	v_lshlrev_b32_e32 v94, 16, v107
	v_lshlrev_b32_e32 v95, 16, v152
	v_lshlrev_b32_e32 v104, 16, v174
	v_lshlrev_b32_e32 v105, 16, v176
	v_lshlrev_b32_e32 v107, 16, v180
	s_waitcnt vmcnt(0)
	v_lshlrev_b32_e32 v109, 16, v182
	s_waitcnt lgkmcnt(0)
; __device__ __forceinline__ float bf2f(bf16 b) { return __uint_as_float(((unsigned)b) << 16); }
; __device__ __forceinline__ bf16 f2bf(float f) { return (bf16)cvt_pk_bf16(f, f); }
; __device__ __forceinline__ int crow(int r, int hi) { return (r & 3) + 8 * (r >> 2) + 4 * hi; }
; template <int PH, bool PRB = false>
; __device__ __forceinline__ void run_phase(int layer, LAS unsigned char* lds, const int wv_) {
;     ...
;                 const int col = g * 128 + 32 * cb0 + r32; bf16 u0[16], u1[16]; float bias[16];
; #pragma unroll
;                 for (int r = 0; r < 16; ++r) { const int prow = 32 * pb + att::crow(r, hi), tok = t0 + prow; bias[r] = bs[g * 128 + prow];
;                     u0[r] = z[(size_t)tok * EVEN_IN + col]; u1[r] = z[(size_t)tok * EVEN_IN + col + 32]; }
; #pragma unroll
;                 for (int r = 0; r < 16; ++r) { const int tok = t0 + 32 * pb + att::crow(r, hi);
;                     y[(size_t)tok * D + col] = f2bf(bf2f(u0[r]) * (acc0[r] + bias[r]));
;                     y[(size_t)tok * D + col + 32] = f2bf(bf2f(u1[r]) * (acc1[r] + bias[r])); }
;             }
;             __syncthreads();
	v_mfma_f32_32x32x16_bf16 v[16:31], v[32:35], v[36:39], v[16:31]
	v_lshlrev_b32_e32 v32, 16, v64
	s_nop 0
	v_add_f32_e32 v0, v0, v52
	v_mul_f32_e32 v0, v0, v32
	v_lshlrev_b32_e32 v33, 16, v160
	v_cvt_pk_bf16_f32 v0, v0, v0
	v_lshlrev_b32_e32 v34, 16, v161
	v_add_f32_e32 v1, v1, v53
	s_nop 4
	v_add_f32_e32 v16, v52, v16
	v_mul_f32_e32 v16, v16, v33
	global_store_short v[56:57], v0, off
	v_cvt_pk_bf16_f32 v0, v16, v16
	v_lshlrev_b32_e32 v35, 16, v162
	v_add_f32_e32 v17, v53, v17
	v_mul_f32_e32 v1, v1, v34
	global_store_short v[56:57], v0, off offset:64
	v_cvt_pk_bf16_f32 v0, v1, v1
	v_lshlrev_b32_e32 v36, 16, v163
	v_add_f32_e32 v2, v2, v54
	v_mul_f32_e32 v17, v17, v35
	global_store_short v[90:91], v0, off
	v_cvt_pk_bf16_f32 v0, v17, v17
	v_lshlrev_b32_e32 v37, 16, v164
	v_add_f32_e32 v18, v54, v18
	v_mul_f32_e32 v2, v2, v36
	global_store_short v[90:91], v0, off offset:64
	v_cvt_pk_bf16_f32 v0, v2, v2
	v_lshlrev_b32_e32 v38, 16, v165
	v_add_f32_e32 v3, v3, v55
	v_mul_f32_e32 v18, v18, v37
	global_store_short v[92:93], v0, off
	v_cvt_pk_bf16_f32 v0, v18, v18
	v_lshlrev_b32_e32 v39, 16, v166
	v_add_f32_e32 v19, v55, v19
	v_mul_f32_e32 v3, v3, v38
	global_store_short v[92:93], v0, off offset:64
	v_cvt_pk_bf16_f32 v0, v3, v3
	v_lshlrev_b32_e32 v52, 16, v167
	v_add_f32_e32 v4, v4, v48
	v_mul_f32_e32 v19, v19, v39
	global_store_short v[86:87], v0, off
	v_cvt_pk_bf16_f32 v0, v19, v19
	v_lshlrev_b32_e32 v53, 16, v168
	v_add_f32_e32 v20, v48, v20
	v_mul_f32_e32 v4, v4, v52
	global_store_short v[86:87], v0, off offset:64
	v_cvt_pk_bf16_f32 v0, v4, v4
	v_lshlrev_b32_e32 v48, 16, v169
	v_add_f32_e32 v5, v5, v49
	v_mul_f32_e32 v20, v20, v53
	global_store_short v[78:79], v0, off
	v_cvt_pk_bf16_f32 v0, v20, v20
	v_lshlrev_b32_e32 v54, 16, v170
	v_add_f32_e32 v21, v49, v21
	v_mul_f32_e32 v5, v5, v48
	global_store_short v[78:79], v0, off offset:64
	v_cvt_pk_bf16_f32 v0, v5, v5
	v_lshlrev_b32_e32 v49, 16, v171
	v_add_f32_e32 v6, v6, v50
	v_mul_f32_e32 v21, v21, v54
	global_store_short v[82:83], v0, off
	v_cvt_pk_bf16_f32 v0, v21, v21
	v_lshlrev_b32_e32 v55, 16, v172
	v_add_f32_e32 v22, v50, v22
	v_mul_f32_e32 v6, v6, v49
	global_store_short v[82:83], v0, off offset:64
	v_cvt_pk_bf16_f32 v0, v6, v6
	v_lshlrev_b32_e32 v50, 16, v150
	v_add_f32_e32 v7, v7, v51
	v_mul_f32_e32 v22, v22, v55
	global_store_short v[40:41], v0, off
	v_cvt_pk_bf16_f32 v0, v22, v22
	v_lshlrev_b32_e32 v64, 16, v151
	v_add_f32_e32 v23, v51, v23
	v_mul_f32_e32 v7, v7, v50
	global_store_short v[40:41], v0, off offset:64
	v_cvt_pk_bf16_f32 v0, v7, v7
	v_lshlrev_b32_e32 v51, 16, v106
	v_add_f32_e32 v8, v8, v100
	v_mul_f32_e32 v23, v23, v64
	global_store_short v[42:43], v0, off
	v_cvt_pk_bf16_f32 v0, v23, v23
	v_add_f32_e32 v24, v100, v24
	v_mul_f32_e32 v8, v8, v51
	global_store_short v[42:43], v0, off offset:64
	v_cvt_pk_bf16_f32 v0, v8, v8
	v_add_f32_e32 v9, v9, v101
	v_mul_f32_e32 v24, v24, v94
	global_store_short v[58:59], v0, off
	v_cvt_pk_bf16_f32 v0, v24, v24
	v_lshlrev_b32_e32 v100, 16, v153
	v_add_f32_e32 v25, v101, v25
	v_mul_f32_e32 v9, v9, v95
	global_store_short v[58:59], v0, off offset:64
	v_cvt_pk_bf16_f32 v0, v9, v9
	v_lshlrev_b32_e32 v101, 16, v173
	v_add_f32_e32 v10, v10, v102
	v_mul_f32_e32 v25, v25, v100
	global_store_short v[76:77], v0, off
	v_cvt_pk_bf16_f32 v0, v25, v25
	v_add_f32_e32 v26, v102, v26
	v_mul_f32_e32 v10, v10, v101
	global_store_short v[76:77], v0, off offset:64
	v_cvt_pk_bf16_f32 v0, v10, v10
	v_lshlrev_b32_e32 v102, 16, v175
	v_add_f32_e32 v11, v11, v103
	v_mul_f32_e32 v26, v26, v104
	global_store_short v[80:81], v0, off
	v_cvt_pk_bf16_f32 v0, v26, v26
	v_add_f32_e32 v27, v103, v27
	v_mul_f32_e32 v11, v11, v102
	global_store_short v[80:81], v0, off offset:64
	v_cvt_pk_bf16_f32 v0, v11, v11
	v_lshlrev_b32_e32 v103, 16, v177
	v_add_f32_e32 v12, v12, v44
	v_mul_f32_e32 v27, v27, v105
	global_store_short v[84:85], v0, off
	v_cvt_pk_bf16_f32 v0, v27, v27
	v_lshlrev_b32_e32 v106, 16, v178
	v_add_f32_e32 v28, v44, v28
	v_mul_f32_e32 v12, v12, v103
	global_store_short v[84:85], v0, off offset:64
	v_cvt_pk_bf16_f32 v0, v12, v12
	v_lshlrev_b32_e32 v44, 16, v179
	v_add_f32_e32 v13, v13, v45
	v_mul_f32_e32 v28, v28, v106
	global_store_short v[88:89], v0, off
	v_cvt_pk_bf16_f32 v0, v28, v28
	v_add_f32_e32 v29, v45, v29
	v_mul_f32_e32 v13, v13, v44
	global_store_short v[88:89], v0, off offset:64
	v_cvt_pk_bf16_f32 v0, v13, v13
	v_lshlrev_b32_e32 v45, 16, v181
	v_add_f32_e32 v14, v14, v46
	v_mul_f32_e32 v29, v29, v107
	global_store_short v[96:97], v0, off
	v_cvt_pk_bf16_f32 v0, v29, v29
	v_add_f32_e32 v30, v46, v30
	v_mul_f32_e32 v14, v14, v45
	global_store_short v[96:97], v0, off offset:64
	v_cvt_pk_bf16_f32 v0, v14, v14
	v_lshlrev_b32_e32 v46, 16, v111
	v_add_f32_e32 v15, v15, v47
	v_mul_f32_e32 v30, v30, v108
	global_store_short v[98:99], v0, off
	v_cvt_pk_bf16_f32 v0, v30, v30
	v_add_f32_e32 v31, v47, v31
	v_mul_f32_e32 v15, v15, v46
	global_store_short v[98:99], v0, off offset:64
	v_cvt_pk_bf16_f32 v0, v15, v15
	v_mul_f32_e32 v31, v31, v109
	global_store_short v[74:75], v0, off
	v_cvt_pk_bf16_f32 v0, v31, v31
	global_store_short v[74:75], v0, off offset:64
	s_barrier
	s_cbranch_scc0 .LBB0_642
